# M3 early flag poll moved one stage earlier (vmcnt(12) at the switch)
# speedup vs baseline: 1.0274x; 1.0061x over previous
.LBB0_1265:
	s_mul_i32 s4, s24, 0xc000
	s_add_i32 s4, s4, 0
	v_add3_u32 v128, s4, v204, v205
	s_barrier
	v_add_u32_e32 v129, 0x4000, v128
	ds_read2_b64 v[136:139], v129 offset1:16
	ds_read2_b64 v[144:147], v129 offset0:128 offset1:144
	v_add_u32_e32 v129, 0x4800, v128
	ds_read2_b64 v[152:155], v129 offset1:16
	ds_read2_b64 v[160:163], v129 offset0:128 offset1:144
	v_add_u32_e32 v129, 0x5000, v128
	v_add_u32_e32 v128, 0x5800, v128
	s_add_i32 s4, s4, s11
	ds_read2_b64 v[168:171], v129 offset1:16
	ds_read2_b64 v[176:179], v129 offset0:128 offset1:144
	ds_read2_b64 v[184:187], v128 offset1:16
	ds_read2_b64 v[188:191], v128 offset0:128 offset1:144
	v_add_u32_e32 v128, s4, v203
	ds_read_b128 v[180:183], v128
	ds_read_b128 v[172:175], v128 offset:1024
	ds_read_b128 v[164:167], v128 offset:2048
	ds_read_b128 v[156:159], v128 offset:3072
	ds_read_b128 v[148:151], v128 offset:4096
	ds_read_b128 v[140:143], v128 offset:5120
	ds_read_b128 v[132:135], v128 offset:6144
	ds_read_b128 v[128:131], v128 offset:7168
	s_cmp_ge_i32 s18, s10
	s_cbranch_scc1 .LBB0_1260
	s_cmp_lg_u32 s6, 14
	s_cbranch_scc1 .Lm3pp_skip
	s_add_i32 s100, s15, 1
	s_cmp_ge_i32 s100, s12
	s_cbranch_scc1 .Lm3pp_skip
	s_mul_i32 s100, s100, 12
	s_add_i32 s100, s100, 0x24190
	v_mov_b32_e32 v214, s100
	ds_read2_b32 v[214:215], v214 offset1:1
	v_mov_b32_e32 v248, 0
	s_waitcnt lgkmcnt(0)
	v_readfirstlane_b32 s100, v214
	v_readfirstlane_b32 s101, v215
	s_lshl_b32 s100, s100, 9
	s_lshl_b32 s101, s101, 4
	s_add_i32 s100, s101, s100
	s_ashr_i32 s101, s100, 31
	s_lshl_b64 s[100:101], s[100:101], 2
	s_add_u32 s100, s20, s100
	s_addc_u32 s101, s21, s101
	global_load_dword v248, v209, s[100:101] sc1
.Lm3pp_skip:
	s_mul_i32 s4, s19, 0xc000
	s_lshl_b32 s5, s6, 6
	s_add_i32 s7, s13, s4
	v_add_u32_e32 v195, s5, v220
	s_mov_b32 m0, s7
	s_lshl_b32 s4, s6, 5
	global_load_lds_dwordx4 v195, s[2:3]
	v_add_u32_e32 v195, s5, v221
	s_ashr_i32 s5, s4, 31
	s_lshl_b64 s[8:9], s[4:5], 13
	v_lshl_add_u64 v[212:213], v[196:197], 0, s[8:9]
	s_or_b32 s8, s4, 8
	s_add_i32 m0, s7, 0x2000
	s_ashr_i32 s9, s8, 31
	global_load_lds_dwordx4 v195, s[2:3]
	s_add_i32 m0, s7, 0x4000
	s_lshl_b64 s[8:9], s[8:9], 13
	global_load_lds_dwordx4 v[212:213], off
	v_lshl_add_u64 v[212:213], v[198:199], 0, s[8:9]
	s_or_b32 s8, s4, 16
	s_ashr_i32 s9, s8, 31
	s_or_b32 s4, s4, 24
	s_add_i32 m0, s7, 0x6000
	s_lshl_b64 s[8:9], s[8:9], 13
	s_ashr_i32 s5, s4, 31
	global_load_lds_dwordx4 v[212:213], off
	v_lshl_add_u64 v[212:213], v[196:197], 0, s[8:9]
	s_add_i32 m0, s7, 0x8000
	s_lshl_b64 s[4:5], s[4:5], 13
	global_load_lds_dwordx4 v[212:213], off
	v_lshl_add_u64 v[212:213], v[198:199], 0, s[4:5]
	s_add_i32 m0, s7, 0xa000
	s_add_i32 s4, s19, 1
	global_load_lds_dwordx4 v[212:213], off
	s_cmp_lg_u32 s19, 2
	s_cselect_b32 s19, s4, 0
	s_add_i32 s6, s6, 1
	s_cmp_lg_u32 s6, 16
	s_cbranch_scc1 .LBB0_1259
	s_add_i32 s15, s15, 1
	s_cmp_ge_i32 s15, s12
	s_cbranch_scc1 .LBB0_1258
	s_mul_i32 s4, s15, 12
	s_add_i32 s4, s4, 0
	s_add_i32 s4, s4, 0x24190
	v_mov_b32_e32 v195, s4
	ds_read2_b32 v[196:197], v195 offset1:1
	ds_read_b32 v195, v195 offset:8
	s_waitcnt lgkmcnt(0)
	v_readfirstlane_b32 s4, v196
	v_readfirstlane_b32 s5, v197
	s_lshl_b32 s6, s4, 9
	s_lshl_b32 s5, s5, 4
	s_add_i32 s6, s5, s6
	s_ashr_i32 s7, s6, 31
	s_lshl_b64 s[6:7], s[6:7], 2
	s_add_u32 s6, s20, s6
	s_addc_u32 s7, s21, s7
	s_waitcnt vmcnt(12)
	v_cmp_lt_u32_e32 vcc, 3, v248
	s_cbranch_vccnz .LBB0_1257
	s_mov_b32 s5, 0x400001
	s_branch .LBB0_1270
